# baseline (speedup 1.0000x reference)
.LBB1_15:
	s_or_b64 exec, exec, s[12:13]
	v_and_b32_e32 v114, 31, v0
	s_mul_i32 s9, s67, 0x60
	s_cmp_lg_u32 s67, 0
	s_cselect_b64 s[74:75], -1, 0
	v_alignbit_b32 v126, v113, v112, 24
	v_cndmask_b32_e64 v126, v112, v126, s[74:75]
	v_bfe_u32 v91, v126, 0, 8
	v_mul_lo_u16_e32 v15, 0x4f, v91
	s_lshl_b32 s7, s66, 3
	v_lshrrev_b16_e32 v15, 9, v15
	s_or_b32 s8, s7, 0xb600
	v_and_b32_e32 v15, 62, v15
	v_add_u32_e32 v15, v91, v15
	s_movk_i32 s6, 0x48
	v_mov_b32_e32 v99, s8
	v_mad_u32_u24 v42, v15, s6, v99
	v_mad_u32_u24 v43, v115, s6, v42
	s_waitcnt lgkmcnt(0)
	s_barrier
	ds_read_b64 v[34:35], v43
	ds_read_b64 v[36:37], v43 offset:8
	ds_read_b64 v[38:39], v43 offset:1080
	ds_read_b64 v[40:41], v43 offset:1088
	v_mov_b32_e32 v2, v46
	v_mov_b32_e32 v3, v46
	v_mov_b32_e32 v4, v46
	v_mov_b32_e32 v5, v46
	v_mov_b32_e32 v6, v47
	v_mov_b32_e32 v7, v47
	v_mov_b32_e32 v8, v47
	v_mov_b32_e32 v9, v47
	v_mov_b32_e32 v10, v48
	v_mov_b32_e32 v11, v48
	v_mov_b32_e32 v12, v48
	v_mov_b32_e32 v13, v48
	v_mov_b32_e32 v14, v49
	v_mov_b32_e32 v15, v49
	v_mov_b32_e32 v16, v49
	v_mov_b32_e32 v17, v49
	s_movk_i32 s8, 0x438
	s_add_i32 s12, s9, 32
	s_waitcnt lgkmcnt(2)
	v_mfma_f32_32x32x16_f16 v[18:33], v[86:89], v[34:37], v[2:17]
	ds_read_b64 v[36:37], v43 offset:2240
	ds_read_b64 v[34:35], v43 offset:2232
	v_and_or_b32 v107, v0, 32, s7
	s_movk_i32 s7, 0x110
	v_mad_u32_u24 v91, v91, s7, v107
	s_add_i32 s9, s9, 64
	s_lshr_b32 s42, s3, 6
	s_waitcnt lgkmcnt(2)
	v_mfma_f32_32x32x16_f16 v[18:33], v[62:65], v[38:41], v[18:33]
	v_mad_u32_u24 v38, v115, s8, v42
	ds_read_b64 v[40:41], v38 offset:152
	ds_read_b64 v[38:39], v38 offset:144
	s_cmpk_lt_u32 s3, 0x100
	s_cselect_b64 s[30:31], -1, 0
	s_add_i32 s13, s69, 0x600
	s_add_i32 s14, s69, 0x700
	v_lshlrev_b32_e32 v116, 4, v115
	s_waitcnt lgkmcnt(2)
	v_mfma_f32_32x32x16_f16 v[18:33], v[58:61], v[34:37], v[18:33]
	ds_read_b64 v[36:37], v43 offset:2168
	ds_read_b64 v[34:35], v43 offset:2160
	s_movk_i32 s15, 0x1070
	s_movk_i32 s16, 0x1ba0
	s_movk_i32 s17, 0x1c20
	s_waitcnt lgkmcnt(2)
	v_mfma_f32_32x32x16_f16 v[18:33], v[54:57], v[38:41], v[18:33]
	v_bfe_u32 v101, v126, 8, 8
	v_mul_lo_u16_e32 v38, 0x4f, v101
	v_lshrrev_b16_e32 v38, 9, v38
	v_and_b32_e32 v38, 62, v38
	v_add_u32_e32 v38, v101, v38
	v_mad_u32_u24 v97, v38, s6, v99
	v_mad_u32_u24 v106, v115, s6, v97
	ds_read_b64 v[92:93], v106
	ds_read_b64 v[94:95], v106 offset:8
	ds_read_b64 v[102:103], v106 offset:2232
	ds_read_b64 v[104:105], v106 offset:2240
	s_waitcnt lgkmcnt(4)
	v_mfma_f32_32x32x16_f16 v[18:33], v[50:53], v[34:37], v[18:33]
	s_add_i32 s12, s69, 0x500
	s_addk_i32 s69, 0x800
	s_cmpk_gt_u32 s3, 0xff
	s_cselect_b64 vcc, -1, 0
	s_waitcnt lgkmcnt(2)
	v_mfma_f32_32x32x16_f16 v[34:49], v[86:89], v[92:95], v[2:17]
	ds_read_b64 v[92:93], v106 offset:1080
	ds_read_b64 v[94:95], v106 offset:1088
	s_nop 4
	v_cvt_pk_f16_f32 v18, v18, v19
	v_pk_max_f16 v96, v18, 0
	v_mad_u32_u24 v18, v115, s8, v97
	v_cvt_pk_f16_f32 v22, v22, v23
	v_cvt_pk_f16_f32 v30, v30, v31
	s_waitcnt lgkmcnt(0)
	v_mfma_f32_32x32x16_f16 v[34:49], v[62:65], v[92:95], v[34:49]
	v_cvt_pk_f16_f32 v92, v20, v21
	ds_read_b64 v[20:21], v18 offset:152
	ds_read_b64 v[18:19], v18 offset:144
	v_pk_max_f16 v97, v92, 0
	ds_read_b64 v[92:93], v106 offset:2160
	ds_read_b64 v[94:95], v106 offset:2168
	v_cvt_pk_f16_f32 v31, v32, v33
	v_mfma_f32_32x32x16_f16 v[34:49], v[58:61], v[102:105], v[34:49]
	v_or_b32_e32 v102, 64, v114
	s_waitcnt lgkmcnt(2)
	v_mfma_f32_32x32x16_f16 v[34:49], v[54:57], v[18:21], v[34:49]
	v_cvt_pk_f16_f32 v19, v24, v25
	v_pk_max_f16 v18, v22, 0
	v_pk_max_f16 v19, v19, 0
	ds_write2_b64 v91, v[96:97], v[18:19] offset1:8
	v_cvt_pk_f16_f32 v18, v26, v27
	v_pk_max_f16 v26, v18, 0
	v_cvt_pk_f16_f32 v22, v28, v29
	v_bfe_u32 v28, v126, 16, 8
	v_mul_lo_u16_e32 v18, 0x4f, v28
	v_lshrrev_b16_e32 v18, 9, v18
	v_and_b32_e32 v18, 62, v18
	v_add_u32_e32 v18, v28, v18
	v_mad_u32_u24 v29, v18, s6, v99
	s_waitcnt lgkmcnt(1)
	v_mfma_f32_32x32x16_f16 v[34:49], v[50:53], v[92:95], v[34:49]
	v_add_u32_e32 v94, s68, v100
	v_add_u32_e32 v94, s69, v94
	v_mov_b32_e32 v95, 0
	v_lshl_add_u64 v[94:95], v[94:95], 4, s[22:23]
	global_load_dwordx4 v[94:97], v[94:95], off
	v_mad_u32_u24 v92, v115, s6, v29
	ds_read_b64 v[18:19], v92
	ds_read_b64 v[20:21], v92 offset:8
	v_pk_max_f16 v27, v22, 0
	ds_read_b64 v[22:23], v92 offset:1080
	ds_read_b64 v[24:25], v92 offset:1088
	v_or_b32_e32 v99, 32, v114
	s_nop 6
	v_cvt_pk_f16_f32 v32, v40, v41
	s_waitcnt lgkmcnt(2)
	v_mfma_f32_32x32x16_f16 v[2:17], v[86:89], v[18:21], v[2:17]
	v_pk_max_f16 v18, v30, 0
	v_pk_max_f16 v19, v31, 0
	ds_write2_b64 v91, v[26:27], v[18:19] offset0:16 offset1:24
	v_cvt_pk_f16_f32 v18, v34, v35
	v_cvt_pk_f16_f32 v19, v36, v37
	v_pk_max_f16 v26, v18, 0
	s_waitcnt lgkmcnt(1)
	v_mfma_f32_32x32x16_f16 v[2:17], v[62:65], v[22:25], v[2:17]
	v_pk_max_f16 v27, v19, 0
	ds_read_b64 v[20:21], v92 offset:2240
	ds_read_b64 v[18:19], v92 offset:2232
	v_mad_u32_u24 v22, v115, s8, v29
	ds_read_b64 v[24:25], v22 offset:152
	ds_read_b64 v[22:23], v22 offset:144
	v_cvt_pk_f16_f32 v31, v38, v39
	v_mad_u32_u24 v30, v101, s7, v107
	s_and_b64 s[8:9], vcc, exec
	s_waitcnt lgkmcnt(2)
	v_mfma_f32_32x32x16_f16 v[2:17], v[58:61], v[18:21], v[2:17]
	v_pk_max_f16 v18, v31, 0
	v_pk_max_f16 v19, v32, 0
	ds_write2_b64 v30, v[26:27], v[18:19] offset1:8
	v_cvt_pk_f16_f32 v18, v42, v43
	v_cvt_pk_f16_f32 v19, v44, v45
	v_pk_max_f16 v26, v18, 0
	s_waitcnt lgkmcnt(1)
	v_mfma_f32_32x32x16_f16 v[2:17], v[54:57], v[22:25], v[2:17]
	v_pk_max_f16 v27, v19, 0
	ds_read_b64 v[20:21], v92 offset:2168
	ds_read_b64 v[18:19], v92 offset:2160
	v_cvt_pk_f16_f32 v22, v46, v47
	v_cvt_pk_f16_f32 v23, v48, v49
	v_pk_max_f16 v22, v22, 0
	v_pk_max_f16 v23, v23, 0
	ds_write2_b64 v30, v[26:27], v[22:23] offset0:16 offset1:24
	s_waitcnt lgkmcnt(1)
	v_mfma_f32_32x32x16_f16 v[2:17], v[50:53], v[18:21], v[2:17]
	v_mad_u32_u24 v18, v28, s7, v107
	v_lshl_or_b32 v42, s66, 5, v116
	s_cselect_b32 s8, 0xf60, 0
	s_movk_i32 s9, 0xff0
	s_cselect_b32 s9, s9, 0x80
	s_cselect_b32 s15, s15, 0x110
	s_cselect_b32 s16, s16, 0x190
	s_nop 4
	v_cvt_pk_f16_f32 v2, v2, v3
	v_cvt_pk_f16_f32 v3, v4, v5
	v_cvt_pk_f16_f32 v4, v6, v7
	v_cvt_pk_f16_f32 v5, v8, v9
	v_pk_max_f16 v2, v2, 0
	v_pk_max_f16 v3, v3, 0
	v_pk_max_f16 v4, v4, 0
	v_pk_max_f16 v5, v5, 0
	ds_write2_b64 v18, v[2:3], v[4:5] offset1:8
	v_cvt_pk_f16_f32 v2, v10, v11
	v_cvt_pk_f16_f32 v3, v12, v13
	v_cvt_pk_f16_f32 v4, v14, v15
	v_cvt_pk_f16_f32 v5, v16, v17
	v_pk_max_f16 v2, v2, 0
	v_pk_max_f16 v3, v3, 0
	v_pk_max_f16 v4, v4, 0
	v_pk_max_f16 v5, v5, 0
	ds_write2_b64 v18, v[2:3], v[4:5] offset0:16 offset1:24
	s_waitcnt vmcnt(0)
	v_bfe_u32 v2, v117, 0, 8
	v_mul_u32_u24_e32 v3, 0xbb, v2
	v_lshrrev_b32_e32 v3, 11, v3
	v_lshl_add_u32 v103, v3, 1, v2
	v_bfe_u32 v2, v117, 8, 8
	v_mul_u32_u24_e32 v3, 0xbb, v2
	v_lshrrev_b32_e32 v3, 11, v3
	v_lshl_add_u32 v106, v3, 1, v2
	v_mad_u32_u24 v90, v103, s7, v42
	v_mad_u32_u24 v91, v106, s7, v42
	v_add_u32_e32 v2, s8, v90
	v_add_u32_e32 v6, s8, v91
	s_waitcnt lgkmcnt(0)
	s_barrier
	ds_read_b128 v[2:5], v2
	ds_read_b128 v[6:9], v6
	s_waitcnt lgkmcnt(1)
	v_mfma_f32_32x32x16_f16 v[18:33], v[82:85], v[2:5], 0
	v_add_u32_e32 v34, s9, v90
	v_add_u32_e32 v38, s9, v91
	ds_read_b128 v[34:37], v34
	ds_read_b128 v[38:41], v38
	s_cselect_b32 s17, s17, 0x220
	v_or_b32_e32 v101, 0x60, v114
	s_waitcnt lgkmcnt(2)
	v_mfma_f32_32x32x16_f16 v[2:17], v[82:85], v[6:9], 0
	s_waitcnt lgkmcnt(1)
	v_mfma_f32_32x32x16_f16 v[18:33], v[74:77], v[34:37], v[18:33]
	v_add_u32_e32 v34, s15, v90
	ds_read_b128 v[34:37], v34
	s_waitcnt lgkmcnt(1)
	v_mfma_f32_32x32x16_f16 v[2:17], v[74:77], v[38:41], v[2:17]
	v_add_u32_e32 v38, s15, v91
	ds_read_b128 v[38:41], v38
	s_waitcnt lgkmcnt(1)
	v_mfma_f32_32x32x16_f16 v[18:33], v[78:81], v[34:37], v[18:33]
	v_add_u32_e32 v34, s16, v90
	ds_read_b128 v[34:37], v34
	s_waitcnt lgkmcnt(1)
	v_mfma_f32_32x32x16_f16 v[2:17], v[78:81], v[38:41], v[2:17]
	v_add_u32_e32 v38, s16, v91
	ds_read_b128 v[38:41], v38
	s_waitcnt lgkmcnt(1)
	v_mfma_f32_32x32x16_f16 v[18:33], v[70:73], v[34:37], v[18:33]
	v_bfe_u32 v43, v117, 16, 8
	v_mul_u32_u24_e32 v34, 0xbb, v43
	v_lshrrev_b32_e32 v104, 11, v34
	v_add_u32_e32 v34, s17, v90
	ds_read_b128 v[34:37], v34
	v_lshl_add_u32 v104, v104, 1, v43
	v_mad_u32_u24 v92, v104, s7, v42
	s_waitcnt lgkmcnt(1)
	v_mfma_f32_32x32x16_f16 v[2:17], v[70:73], v[38:41], v[2:17]
	v_add_u32_e32 v38, s17, v91
	ds_read_b128 v[38:41], v38
	s_waitcnt lgkmcnt(1)
	v_mfma_f32_32x32x16_f16 v[18:33], v[66:69], v[34:37], v[18:33]
	v_bfe_u32 v34, v117, 24, 8
	v_mul_u32_u24_e32 v35, 0xbb, v34
	v_lshrrev_b32_e32 v35, 11, v35
	v_lshl_add_u32 v105, v35, 1, v34
	v_mad_u32_u24 v93, v105, s7, v42
	s_waitcnt lgkmcnt(0)
	v_mfma_f32_32x32x16_f16 v[2:17], v[66:69], v[38:41], v[2:17]
	v_add_u32_e32 v34, s8, v92
	v_add_u32_e32 v38, s8, v93
	ds_read_b128 v[34:37], v34
	ds_read_b128 v[38:41], v38
	v_add_u32_e32 v86, s9, v93
	s_waitcnt lgkmcnt(1)
	v_mfma_f32_32x32x16_f16 v[50:65], v[82:85], v[34:37], 0
	ds_read_b128 v[86:89], v86
	s_waitcnt lgkmcnt(1)
	v_mfma_f32_32x32x16_f16 v[34:49], v[82:85], v[38:41], 0
	v_add_u32_e32 v82, s9, v92
	ds_read_b128 v[82:85], v82
	s_waitcnt lgkmcnt(0)
	v_mfma_f32_32x32x16_f16 v[50:65], v[74:77], v[82:85], v[50:65]
	v_add_u32_e32 v82, s15, v93
	ds_read_b128 v[82:85], v82
	v_mfma_f32_32x32x16_f16 v[34:49], v[74:77], v[86:89], v[34:49]
	v_add_u32_e32 v74, s15, v92
	ds_read_b128 v[74:77], v74
	s_waitcnt lgkmcnt(0)
	v_mfma_f32_32x32x16_f16 v[50:65], v[78:81], v[74:77], v[50:65]
	v_add_u32_e32 v74, s16, v92
	ds_read_b128 v[74:77], v74
	v_mfma_f32_32x32x16_f16 v[34:49], v[78:81], v[82:85], v[34:49]
	v_add_u32_e32 v78, s16, v93
	ds_read_b128 v[78:81], v78
	s_waitcnt lgkmcnt(1)
	v_mfma_f32_32x32x16_f16 v[50:65], v[70:73], v[74:77], v[50:65]
	v_add_u32_e32 v74, s17, v93
	ds_read_b128 v[74:77], v74
	s_waitcnt lgkmcnt(1)
	v_mfma_f32_32x32x16_f16 v[34:49], v[70:73], v[78:81], v[34:49]
	v_add_u32_e32 v70, s17, v92
	ds_read_b128 v[70:73], v70
	s_waitcnt lgkmcnt(0)
	v_mfma_f32_32x32x16_f16 v[50:65], v[66:69], v[70:73], v[50:65]
	v_mfma_f32_32x32x16_f16 v[34:49], v[66:69], v[74:77], v[34:49]
	s_movk_i32 s7, 0x1cb0
	s_cselect_b32 s7, s7, 0x2a0
	v_add_u32_e32 v74, s7, v90
	ds_read_b128 v[74:77], v74
	v_add_u32_e32 v78, s7, v91
	ds_read_b128 v[78:81], v78
	s_movk_i32 s12, 0x1d30
	s_cselect_b32 s12, s12, 0xdd0
	s_movk_i32 s8, 0x1dc0
	s_cselect_b32 s8, s8, 0xe50
	s_movk_i32 s9, 0x1e40
	s_cselect_b32 s9, s9, 0xee0
	s_waitcnt vmcnt(0) lgkmcnt(1)
	v_mfma_f32_32x32x16_f16 v[18:33], v[108:111], v[74:77], v[18:33]
	v_add_u32_e32 v82, s12, v91
	ds_read_b128 v[82:85], v82
	s_waitcnt lgkmcnt(1)
	v_mfma_f32_32x32x16_f16 v[2:17], v[108:111], v[78:81], v[2:17]
	v_add_u32_e32 v78, s12, v90
	ds_read_b128 v[78:81], v78
	s_waitcnt lgkmcnt(0)
	v_mfma_f32_32x32x16_f16 v[18:33], v[118:121], v[78:81], v[18:33]
	v_add_u32_e32 v86, s8, v91
	ds_read_b128 v[86:89], v86
	v_mfma_f32_32x32x16_f16 v[2:17], v[118:121], v[82:85], v[2:17]
	v_add_u32_e32 v82, s8, v90
	ds_read_b128 v[82:85], v82
	s_waitcnt lgkmcnt(0)
	v_mfma_f32_32x32x16_f16 v[18:33], v[122:125], v[82:85], v[18:33]
	v_add_u32_e32 v82, s9, v90
	ds_read_b128 v[82:85], v82
	v_mfma_f32_32x32x16_f16 v[2:17], v[122:125], v[86:89], v[2:17]
	v_add_u32_e32 v86, s9, v91
	ds_read_b128 v[86:89], v86
	s_waitcnt lgkmcnt(1)
	v_mfma_f32_32x32x16_f16 v[18:33], v[94:97], v[82:85], v[18:33]
	s_waitcnt lgkmcnt(0)
	v_mfma_f32_32x32x16_f16 v[2:17], v[94:97], v[86:89], v[2:17]
	v_add_u32_e32 v82, s7, v92
	v_add_u32_e32 v86, s7, v93
	ds_read_b128 v[82:85], v82
	ds_read_b128 v[86:89], v86
	s_waitcnt lgkmcnt(1)
	v_mfma_f32_32x32x16_f16 v[50:65], v[108:111], v[82:85], v[50:65]
	v_add_u32_e32 v82, s12, v93
	ds_read_b128 v[82:85], v82
	s_waitcnt lgkmcnt(1)
	v_mfma_f32_32x32x16_f16 v[34:49], v[108:111], v[86:89], v[34:49]
	v_add_u32_e32 v66, s12, v92
	ds_read_b128 v[66:69], v66
	s_waitcnt lgkmcnt(0)
	v_mfma_f32_32x32x16_f16 v[50:65], v[118:121], v[66:69], v[50:65]
	v_add_u32_e32 v66, s8, v92
	ds_read_b128 v[66:69], v66
	v_mfma_f32_32x32x16_f16 v[34:49], v[118:121], v[82:85], v[34:49]
	v_add_u32_e32 v70, s8, v93
	ds_read_b128 v[70:73], v70
	s_waitcnt lgkmcnt(1)
	v_mfma_f32_32x32x16_f16 v[50:65], v[122:125], v[66:69], v[50:65]
	v_add_u32_e32 v66, s9, v92
	ds_read_b128 v[66:69], v66
	s_waitcnt lgkmcnt(1)
	v_mfma_f32_32x32x16_f16 v[34:49], v[122:125], v[70:73], v[34:49]
	v_add_u32_e32 v70, s9, v93
	ds_read_b128 v[70:73], v70
	s_waitcnt lgkmcnt(1)
	v_mfma_f32_32x32x16_f16 v[50:65], v[94:97], v[66:69], v[50:65]
	s_waitcnt lgkmcnt(0)
	v_mfma_f32_32x32x16_f16 v[34:49], v[94:97], v[70:73], v[34:49]
	s_cmpk_gt_u32 s3, 0x17f
	s_barrier
	s_cbranch_scc1 .LBB1_17
	s_mul_hi_u32 s7, s42, 0x55555556
	s_mul_i32 s7, s7, 3
	s_sub_i32 s7, s42, s7
	s_lshl_b32 s7, s7, 3
	s_add_i32 s8, s7, 0xb600
	s_cmpk_gt_u32 s3, 0xbf
	s_cselect_b64 s[74:75], -1, 0
	s_movk_i32 s12, 0x438
	s_movk_i32 s13, 0xd0
	v_alignbit_b32 v99, v113, v112, 24
	v_cndmask_b32_e64 v99, v112, v99, s[74:75]
	v_add_u32_e32 v122, 0xf550, v98
	ds_read_b128 v[82:85], v98 offset:62800
	ds_read_b128 v[86:89], v98 offset:63824
	ds_read_b128 v[90:93], v98 offset:64848
	ds_read_b128 v[94:97], v122 offset:3072
	ds_read_b128 v[118:121], v122 offset:4096
	ds_read_b32 v107, v122 offset:5120
	ds_read_b32 v112, v122 offset:5124
	ds_read_b32 v113, v122 offset:5128
	ds_read_b32 v117, v122 offset:5132
	v_bfe_u32 v101, v99, 0, 8
	v_mul_lo_u16_e32 v102, 0x4f, v101
	v_lshrrev_b16_e32 v102, 9, v102
	v_and_b32_e32 v102, 62, v102
	v_add_u32_e32 v102, v101, v102
	v_mov_b32_e32 v123, s8
	v_mad_u32_u24 v102, v102, s6, v123
	v_mad_u32_u24 v123, v115, s6, v102
	v_mad_u32_u24 v102, v115, s12, v102
	v_mad_u32_u24 v122, v115, 24, s7
	v_mad_u32_u24 v101, v101, s13, v122
	ds_read_b64 v[108:109], v123 offset:32
	ds_read_b64 v[110:111], v123 offset:40
	ds_read_b64 v[124:125], v123 offset:1112
	ds_read_b64 v[126:127], v123 offset:1120
	s_waitcnt lgkmcnt(2)
	v_mfma_f32_32x32x16_f16 v[66:81], v[82:85], v[108:111], 0
	ds_read_b64 v[108:109], v123 offset:2264
	ds_read_b64 v[110:111], v123 offset:2272
	s_waitcnt lgkmcnt(2)
	v_mfma_f32_32x32x16_f16 v[66:81], v[86:89], v[124:127], v[66:81]
	ds_read_b64 v[124:125], v102 offset:176
	ds_read_b64 v[126:127], v102 offset:184
	s_waitcnt lgkmcnt(2)
	v_mfma_f32_32x32x16_f16 v[66:81], v[90:93], v[108:111], v[66:81]
	ds_read_b64 v[108:109], v123 offset:2192
	ds_read_b64 v[110:111], v123 offset:2200
	s_waitcnt lgkmcnt(2)
	v_mfma_f32_32x32x16_f16 v[66:81], v[94:97], v[124:127], v[66:81]
	s_waitcnt lgkmcnt(0)
	v_mfma_f32_32x32x16_f16 v[66:81], v[118:121], v[108:111], v[66:81]
	v_bfe_u32 v124, v99, 8, 8
	v_mul_lo_u16_e32 v126, 0x4f, v124
	v_lshrrev_b16_e32 v126, 9, v126
	v_and_b32_e32 v126, 62, v126
	v_add_u32_e32 v126, v124, v126
	v_mov_b32_e32 v123, s8
	v_mad_u32_u24 v126, v126, s6, v123
	v_mad_u32_u24 v123, v115, s6, v126
	v_mad_u32_u24 v102, v115, s12, v126
	ds_read_b64 v[108:109], v123 offset:32
	ds_read_b64 v[110:111], v123 offset:40
	ds_read_b64 v[124:125], v123 offset:1112
	ds_read_b64 v[126:127], v123 offset:1120
	v_add_f32_e32 v66, v107, v66
	v_add_f32_e32 v67, v107, v67
	v_add_f32_e32 v68, v107, v68
	v_add_f32_e32 v69, v107, v69
	v_add_f32_e32 v70, v112, v70
	v_add_f32_e32 v71, v112, v71
	v_add_f32_e32 v72, v112, v72
	v_add_f32_e32 v73, v112, v73
	v_add_f32_e32 v74, v113, v74
	v_add_f32_e32 v75, v113, v75
	v_add_f32_e32 v76, v113, v76
	v_add_f32_e32 v77, v113, v77
	v_add_f32_e32 v78, v117, v78
	v_add_f32_e32 v79, v117, v79
	v_add_f32_e32 v80, v117, v80
	v_add_f32_e32 v81, v117, v81
	v_cvt_pk_f16_f32 v66, v66, v67
	v_cvt_pk_f16_f32 v67, v68, v69
	v_cvt_pk_f16_f32 v68, v70, v71
	v_cvt_pk_f16_f32 v69, v72, v73
	v_cvt_pk_f16_f32 v70, v74, v75
	v_cvt_pk_f16_f32 v71, v76, v77
	v_cvt_pk_f16_f32 v72, v78, v79
	v_cvt_pk_f16_f32 v73, v80, v81
	v_pk_max_f16 v66, v66, 0
	v_pk_max_f16 v67, v67, 0
	v_pk_max_f16 v68, v68, 0
	v_pk_max_f16 v69, v69, 0
	v_pk_max_f16 v70, v70, 0
	v_pk_max_f16 v71, v71, 0
	v_pk_max_f16 v72, v72, 0
	v_pk_max_f16 v73, v73, 0
	ds_write2_b64 v101, v[66:67], v[68:69] offset1:6
	ds_write2_b64 v101, v[70:71], v[72:73] offset0:12 offset1:18
	v_bfe_u32 v101, v99, 8, 8
	v_mad_u32_u24 v122, v115, 24, s7
	v_mad_u32_u24 v101, v101, s13, v122
	s_waitcnt lgkmcnt(4)
	v_mfma_f32_32x32x16_f16 v[66:81], v[82:85], v[108:111], 0
	ds_read_b64 v[108:109], v123 offset:2264
	ds_read_b64 v[110:111], v123 offset:2272
	s_waitcnt lgkmcnt(2)
	v_mfma_f32_32x32x16_f16 v[66:81], v[86:89], v[124:127], v[66:81]
	ds_read_b64 v[124:125], v102 offset:176
	ds_read_b64 v[126:127], v102 offset:184
	s_waitcnt lgkmcnt(2)
	v_mfma_f32_32x32x16_f16 v[66:81], v[90:93], v[108:111], v[66:81]
	ds_read_b64 v[108:109], v123 offset:2192
	ds_read_b64 v[110:111], v123 offset:2200
	s_waitcnt lgkmcnt(2)
	v_mfma_f32_32x32x16_f16 v[66:81], v[94:97], v[124:127], v[66:81]
	s_waitcnt lgkmcnt(0)
	v_mfma_f32_32x32x16_f16 v[66:81], v[118:121], v[108:111], v[66:81]
	v_bfe_u32 v124, v99, 16, 8
	v_mul_lo_u16_e32 v126, 0x4f, v124
	v_lshrrev_b16_e32 v126, 9, v126
	v_and_b32_e32 v126, 62, v126
	v_add_u32_e32 v126, v124, v126
	v_mov_b32_e32 v123, s8
	v_mad_u32_u24 v126, v126, s6, v123
	v_mad_u32_u24 v123, v115, s6, v126
	v_mad_u32_u24 v102, v115, s12, v126
	ds_read_b64 v[108:109], v123 offset:32
	ds_read_b64 v[110:111], v123 offset:40
	ds_read_b64 v[124:125], v123 offset:1112
	ds_read_b64 v[126:127], v123 offset:1120
	v_add_f32_e32 v66, v107, v66
	v_add_f32_e32 v67, v107, v67
	v_add_f32_e32 v68, v107, v68
	v_add_f32_e32 v69, v107, v69
	v_add_f32_e32 v70, v112, v70
	v_add_f32_e32 v71, v112, v71
	v_add_f32_e32 v72, v112, v72
	v_add_f32_e32 v73, v112, v73
	v_add_f32_e32 v74, v113, v74
	v_add_f32_e32 v75, v113, v75
	v_add_f32_e32 v76, v113, v76
	v_add_f32_e32 v77, v113, v77
	v_add_f32_e32 v78, v117, v78
	v_add_f32_e32 v79, v117, v79
	v_add_f32_e32 v80, v117, v80
	v_add_f32_e32 v81, v117, v81
	v_cvt_pk_f16_f32 v66, v66, v67
	v_cvt_pk_f16_f32 v67, v68, v69
	v_cvt_pk_f16_f32 v68, v70, v71
	v_cvt_pk_f16_f32 v69, v72, v73
	v_cvt_pk_f16_f32 v70, v74, v75
	v_cvt_pk_f16_f32 v71, v76, v77
	v_cvt_pk_f16_f32 v72, v78, v79
	v_cvt_pk_f16_f32 v73, v80, v81
	v_pk_max_f16 v66, v66, 0
	v_pk_max_f16 v67, v67, 0
	v_pk_max_f16 v68, v68, 0
	v_pk_max_f16 v69, v69, 0
	v_pk_max_f16 v70, v70, 0
	v_pk_max_f16 v71, v71, 0
	v_pk_max_f16 v72, v72, 0
	v_pk_max_f16 v73, v73, 0
	ds_write2_b64 v101, v[66:67], v[68:69] offset1:6
	ds_write2_b64 v101, v[70:71], v[72:73] offset0:12 offset1:18
	v_bfe_u32 v101, v99, 16, 8
	v_mad_u32_u24 v122, v115, 24, s7
	v_mad_u32_u24 v101, v101, s13, v122
	s_waitcnt lgkmcnt(4)
	v_mfma_f32_32x32x16_f16 v[66:81], v[82:85], v[108:111], 0
	ds_read_b64 v[108:109], v123 offset:2264
	ds_read_b64 v[110:111], v123 offset:2272
	s_waitcnt lgkmcnt(2)
	v_mfma_f32_32x32x16_f16 v[66:81], v[86:89], v[124:127], v[66:81]
	ds_read_b64 v[124:125], v102 offset:176
	ds_read_b64 v[126:127], v102 offset:184
	s_waitcnt lgkmcnt(2)
	v_mfma_f32_32x32x16_f16 v[66:81], v[90:93], v[108:111], v[66:81]
	ds_read_b64 v[108:109], v123 offset:2192
	ds_read_b64 v[110:111], v123 offset:2200
	s_waitcnt lgkmcnt(2)
	v_mfma_f32_32x32x16_f16 v[66:81], v[94:97], v[124:127], v[66:81]
	s_waitcnt lgkmcnt(0)
	v_mfma_f32_32x32x16_f16 v[66:81], v[118:121], v[108:111], v[66:81]
	v_or_b32_e32 v99, 32, v114
	v_or_b32_e32 v102, 64, v114
	s_nop 9
	v_add_f32_e32 v66, v107, v66
	v_add_f32_e32 v67, v107, v67
	v_add_f32_e32 v68, v107, v68
	v_add_f32_e32 v69, v107, v69
	v_add_f32_e32 v70, v112, v70
	v_add_f32_e32 v71, v112, v71
	v_add_f32_e32 v72, v112, v72
	v_add_f32_e32 v73, v112, v73
	v_add_f32_e32 v74, v113, v74
	v_add_f32_e32 v75, v113, v75
	v_add_f32_e32 v76, v113, v76
	v_add_f32_e32 v77, v113, v77
	v_add_f32_e32 v78, v117, v78
	v_add_f32_e32 v79, v117, v79
	v_add_f32_e32 v80, v117, v80
	v_add_f32_e32 v81, v117, v81
	v_cvt_pk_f16_f32 v66, v66, v67
	v_cvt_pk_f16_f32 v67, v68, v69
	v_cvt_pk_f16_f32 v68, v70, v71
	v_cvt_pk_f16_f32 v69, v72, v73
	v_cvt_pk_f16_f32 v70, v74, v75
	v_cvt_pk_f16_f32 v71, v76, v77
	v_cvt_pk_f16_f32 v72, v78, v79
	v_cvt_pk_f16_f32 v73, v80, v81
	v_pk_max_f16 v66, v66, 0
	v_pk_max_f16 v67, v67, 0
	v_pk_max_f16 v68, v68, 0
	v_pk_max_f16 v69, v69, 0
	v_pk_max_f16 v70, v70, 0
	v_pk_max_f16 v71, v71, 0
	v_pk_max_f16 v72, v72, 0
	v_pk_max_f16 v73, v73, 0
	ds_write2_b64 v101, v[66:67], v[68:69] offset1:6
	ds_write2_b64 v101, v[70:71], v[72:73] offset0:12 offset1:18
	v_or_b32_e32 v101, 0x60, v114
